# bf16 GEMM K-loops: B-fragment ds_reads moved from the load segments into the preceding MFMA segment (woven behind the MFMAs), counted vmcnt(8) one phase earlier; on top of v062
# baseline (speedup 1.0000x reference)
.LBB0_619:
	s_ashr_i32 s21, s20, 31
	v_cmp_lt_i64_e32 vcc, s[22:23], v[142:143]
	s_lshl_b64 s[22:23], s[20:21], 20
	v_readlane_b32 s19, v254, 36
	s_add_u32 s22, s19, s22
	v_readlane_b32 s19, v254, 37
	s_addc_u32 s23, s19, s23
	s_and_b64 s[26:27], vcc, exec
	s_cselect_b32 s21, s23, s29
	s_cselect_b32 s54, s22, s28
	s_ashr_i32 s19, s18, 31
	s_lshl_b64 s[26:27], s[18:19], 20
	s_add_u32 s26, s33, s26
	s_addc_u32 s27, s36, s27
	s_and_b64 s[34:35], vcc, exec
	s_cselect_b32 s19, s27, s31
	s_cselect_b32 s55, s26, s30
	s_add_u32 s28, s28, 0x80080
	s_addc_u32 s29, s29, 0
	s_add_u32 s56, s30, 0x100
	v_mov_b32_e32 v2, 0
	s_addc_u32 s57, s31, 0
	s_mov_b32 s60, -2
	v_mov_b32_e32 v3, v2
	v_mov_b32_e32 v4, v2
	v_mov_b32_e32 v5, v2
	v_mov_b32_e32 v6, v2
	v_mov_b32_e32 v7, v2
	v_mov_b32_e32 v8, v2
	v_mov_b32_e32 v9, v2
	v_mov_b32_e32 v10, v2
	v_mov_b32_e32 v11, v2
	v_mov_b32_e32 v12, v2
	v_mov_b32_e32 v13, v2
	v_mov_b32_e32 v14, v2
	v_mov_b32_e32 v15, v2
	v_mov_b32_e32 v16, v2
	v_mov_b32_e32 v17, v2
	v_mov_b32_e32 v26, v2
	v_mov_b32_e32 v27, v2
	v_mov_b32_e32 v28, v2
	v_mov_b32_e32 v29, v2
	v_mov_b32_e32 v30, v2
	v_mov_b32_e32 v31, v2
	v_mov_b32_e32 v32, v2
	v_mov_b32_e32 v33, v2
	v_mov_b32_e32 v42, v2
	v_mov_b32_e32 v43, v2
	v_mov_b32_e32 v44, v2
	v_mov_b32_e32 v45, v2
	v_mov_b32_e32 v46, v2
	v_mov_b32_e32 v47, v2
	v_mov_b32_e32 v48, v2
	v_mov_b32_e32 v49, v2
	v_mov_b32_e32 v18, v2
	v_mov_b32_e32 v19, v2
	v_mov_b32_e32 v20, v2
	v_mov_b32_e32 v21, v2
	v_mov_b32_e32 v22, v2
	v_mov_b32_e32 v23, v2
	v_mov_b32_e32 v24, v2
	v_mov_b32_e32 v25, v2
	v_mov_b32_e32 v34, v2
	v_mov_b32_e32 v35, v2
	v_mov_b32_e32 v36, v2
	v_mov_b32_e32 v37, v2
	v_mov_b32_e32 v38, v2
	v_mov_b32_e32 v39, v2
	v_mov_b32_e32 v40, v2
	v_mov_b32_e32 v41, v2
	v_mov_b32_e32 v50, v2
	v_mov_b32_e32 v51, v2
	v_mov_b32_e32 v52, v2
	v_mov_b32_e32 v53, v2
	v_mov_b32_e32 v54, v2
	v_mov_b32_e32 v55, v2
	v_mov_b32_e32 v56, v2
	v_mov_b32_e32 v57, v2
	v_mov_b32_e32 v58, v2
	v_mov_b32_e32 v59, v2
	v_mov_b32_e32 v60, v2
	v_mov_b32_e32 v61, v2
	v_mov_b32_e32 v62, v2
	v_mov_b32_e32 v63, v2
	v_mov_b32_e32 v64, v2
	v_mov_b32_e32 v65, v2
	v_mov_b32_e32 v66, v2
	v_mov_b32_e32 v67, v2
	v_mov_b32_e32 v68, v2
	v_mov_b32_e32 v69, v2
	v_mov_b32_e32 v70, v2
	v_mov_b32_e32 v71, v2
	v_mov_b32_e32 v72, v2
	v_mov_b32_e32 v73, v2
	v_mov_b32_e32 v74, v2
	v_mov_b32_e32 v75, v2
	v_mov_b32_e32 v76, v2
	v_mov_b32_e32 v77, v2
	v_mov_b32_e32 v78, v2
	v_mov_b32_e32 v79, v2
	v_mov_b32_e32 v80, v2
	v_mov_b32_e32 v81, v2
	v_mov_b32_e32 v90, v2
	v_mov_b32_e32 v91, v2
	v_mov_b32_e32 v92, v2
	v_mov_b32_e32 v93, v2
	v_mov_b32_e32 v94, v2
	v_mov_b32_e32 v95, v2
	v_mov_b32_e32 v96, v2
	v_mov_b32_e32 v97, v2
	v_mov_b32_e32 v106, v2
	v_mov_b32_e32 v107, v2
	v_mov_b32_e32 v108, v2
	v_mov_b32_e32 v109, v2
	v_mov_b32_e32 v110, v2
	v_mov_b32_e32 v111, v2
	v_mov_b32_e32 v112, v2
	v_mov_b32_e32 v113, v2
	v_mov_b32_e32 v82, v2
	v_mov_b32_e32 v83, v2
	v_mov_b32_e32 v84, v2
	v_mov_b32_e32 v85, v2
	v_mov_b32_e32 v86, v2
	v_mov_b32_e32 v87, v2
	v_mov_b32_e32 v88, v2
	v_mov_b32_e32 v89, v2
	v_mov_b32_e32 v98, v2
	v_mov_b32_e32 v99, v2
	v_mov_b32_e32 v100, v2
	v_mov_b32_e32 v101, v2
	v_mov_b32_e32 v102, v2
	v_mov_b32_e32 v103, v2
	v_mov_b32_e32 v104, v2
	v_mov_b32_e32 v105, v2
	v_mov_b32_e32 v114, v2
	v_mov_b32_e32 v115, v2
	v_mov_b32_e32 v116, v2
	v_mov_b32_e32 v117, v2
	v_mov_b32_e32 v118, v2
	v_mov_b32_e32 v119, v2
	v_mov_b32_e32 v120, v2
	v_mov_b32_e32 v121, v2
	v_mov_b32_e32 v122, v2
	v_mov_b32_e32 v123, v2
	v_mov_b32_e32 v124, v2
	v_mov_b32_e32 v125, v2
	v_mov_b32_e32 v126, v2
	v_mov_b32_e32 v127, v2
	v_mov_b32_e32 v128, v2
	v_mov_b32_e32 v129, v2
	ds_read_b128 v[152:155], v148
	ds_read_b128 v[156:159], v148 offset:1024
	ds_read_b128 v[160:163], v148 offset:2048
	ds_read_b128 v[164:167], v148 offset:3072
.LBB0_620:
	s_add_u32 s30, s28, 0xfff80080
	s_addc_u32 s31, s29, -1
	s_cmp_eq_u32 s60, 28
	s_cselect_b32 s35, s21, s31
	s_cselect_b32 s34, s54, s30
	s_cselect_b32 s31, s19, s57
	s_cselect_b32 s30, s55, s56
	s_add_i32 m0, s17, 0xc000
	ds_read_b128 v[168:171], v149
	ds_read_b128 v[172:175], v149 offset:1024
	ds_read_b128 v[176:179], v149 offset:2048
	ds_read_b128 v[180:183], v149 offset:3072
	ds_read_b128 v[184:187], v149 offset:4096
	ds_read_b128 v[188:191], v149 offset:5120
	ds_read_b128 v[192:195], v149 offset:6144
	ds_read_b128 v[196:199], v149 offset:7168
	global_load_lds_dwordx4 v138, s[28:29]
	s_add_i32 m0, s17, 0xe000
	s_nop 0
	global_load_lds_dwordx4 v140, s[28:29]
	s_barrier
	s_waitcnt lgkmcnt(0)
	s_setprio 1
	s_waitcnt lgkmcnt(0)
	v_mfma_f32_16x16x32_bf16 v[126:129], v[152:155], v[168:171], v[126:129]
	v_mfma_f32_16x16x32_bf16 v[122:125], v[160:163], v[168:171], v[122:125]
	ds_read_b128 v[200:203], v150
	v_mfma_f32_16x16x32_bf16 v[118:121], v[152:155], v[176:179], v[118:121]
	v_mfma_f32_16x16x32_bf16 v[114:117], v[160:163], v[176:179], v[114:117]
	ds_read_b128 v[206:209], v150 offset:1024
	v_mfma_f32_16x16x32_bf16 v[102:105], v[152:155], v[184:187], v[102:105]
	v_mfma_f32_16x16x32_bf16 v[98:101], v[160:163], v[184:187], v[98:101]
	ds_read_b128 v[210:213], v150 offset:2048
	v_mfma_f32_16x16x32_bf16 v[86:89], v[152:155], v[192:195], v[86:89]
	v_mfma_f32_16x16x32_bf16 v[82:85], v[160:163], v[192:195], v[82:85]
	ds_read_b128 v[214:217], v150 offset:3072
	v_mfma_f32_16x16x32_bf16 v[126:129], v[156:159], v[172:175], v[126:129]
	v_mfma_f32_16x16x32_bf16 v[122:125], v[164:167], v[172:175], v[122:125]
	v_mfma_f32_16x16x32_bf16 v[118:121], v[156:159], v[180:183], v[118:121]
	v_mfma_f32_16x16x32_bf16 v[114:117], v[164:167], v[180:183], v[114:117]
	v_mfma_f32_16x16x32_bf16 v[102:105], v[156:159], v[188:191], v[102:105]
	v_mfma_f32_16x16x32_bf16 v[98:101], v[164:167], v[188:191], v[98:101]
	v_mfma_f32_16x16x32_bf16 v[86:89], v[156:159], v[196:199], v[86:89]
	v_mfma_f32_16x16x32_bf16 v[82:85], v[164:167], v[196:199], v[82:85]
	s_setprio 0
	s_barrier
	s_add_i32 s61, s47, s37
	s_add_u32 s66, s30, 0x80
	s_addc_u32 s67, s31, 0
	s_mov_b32 m0, s61
	global_load_lds_dwordx4 v134, s[30:31]
	s_add_i32 m0, s61, 0x2000
	s_nop 0
	global_load_lds_dwordx4 v130, s[30:31]
	s_barrier
	s_waitcnt lgkmcnt(0)
	s_setprio 1
	s_waitcnt lgkmcnt(0)
	v_mfma_f32_16x16x32_bf16 v[110:113], v[200:203], v[168:171], v[110:113]
	v_mfma_f32_16x16x32_bf16 v[106:109], v[210:213], v[168:171], v[106:109]
	v_mfma_f32_16x16x32_bf16 v[94:97], v[200:203], v[176:179], v[94:97]
	v_mfma_f32_16x16x32_bf16 v[90:93], v[210:213], v[176:179], v[90:93]
	v_mfma_f32_16x16x32_bf16 v[78:81], v[200:203], v[184:187], v[78:81]
	v_mfma_f32_16x16x32_bf16 v[74:77], v[210:213], v[184:187], v[74:77]
	v_mfma_f32_16x16x32_bf16 v[70:73], v[200:203], v[192:195], v[70:73]
	v_mfma_f32_16x16x32_bf16 v[66:69], v[210:213], v[192:195], v[66:69]
	v_mfma_f32_16x16x32_bf16 v[110:113], v[206:209], v[172:175], v[110:113]
	v_mfma_f32_16x16x32_bf16 v[106:109], v[214:217], v[172:175], v[106:109]
	v_mfma_f32_16x16x32_bf16 v[94:97], v[206:209], v[180:183], v[94:97]
	v_mfma_f32_16x16x32_bf16 v[90:93], v[214:217], v[180:183], v[90:93]
	v_mfma_f32_16x16x32_bf16 v[78:81], v[206:209], v[188:191], v[78:81]
	v_mfma_f32_16x16x32_bf16 v[74:77], v[214:217], v[188:191], v[74:77]
	v_mfma_f32_16x16x32_bf16 v[70:73], v[206:209], v[196:199], v[70:73]
	v_mfma_f32_16x16x32_bf16 v[66:69], v[214:217], v[196:199], v[66:69]
	s_setprio 0
	s_mov_b32 m0, s17
	s_add_u32 s68, s34, 0x80
	s_addc_u32 s69, s35, 0
	s_barrier
	ds_read_b128 v[168:171], v149 offset:16384
	ds_read_b128 v[172:175], v149 offset:17408
	ds_read_b128 v[176:179], v149 offset:18432
	ds_read_b128 v[180:183], v149 offset:19456
	ds_read_b128 v[184:187], v149 offset:20480
	ds_read_b128 v[188:191], v149 offset:21504
	ds_read_b128 v[192:195], v149 offset:22528
	ds_read_b128 v[196:199], v149 offset:23552
	global_load_lds_dwordx4 v136, s[34:35]
	s_mov_b32 m0, s40
	s_nop 0
	global_load_lds_dwordx4 v132, s[34:35]
	s_waitcnt vmcnt(8)
	s_barrier
	s_waitcnt lgkmcnt(0)
	s_setprio 1
	s_waitcnt lgkmcnt(0)
	v_mfma_f32_16x16x32_bf16 v[62:65], v[152:155], v[168:171], v[62:65]
	v_mfma_f32_16x16x32_bf16 v[58:61], v[160:163], v[168:171], v[58:61]
	v_mfma_f32_16x16x32_bf16 v[54:57], v[152:155], v[176:179], v[54:57]
	v_mfma_f32_16x16x32_bf16 v[50:53], v[160:163], v[176:179], v[50:53]
	v_mfma_f32_16x16x32_bf16 v[38:41], v[152:155], v[184:187], v[38:41]
	v_mfma_f32_16x16x32_bf16 v[34:37], v[160:163], v[184:187], v[34:37]
	v_mfma_f32_16x16x32_bf16 v[22:25], v[152:155], v[192:195], v[22:25]
	v_mfma_f32_16x16x32_bf16 v[18:21], v[160:163], v[192:195], v[18:21]
	v_mfma_f32_16x16x32_bf16 v[62:65], v[156:159], v[172:175], v[62:65]
	v_mfma_f32_16x16x32_bf16 v[58:61], v[164:167], v[172:175], v[58:61]
	v_mfma_f32_16x16x32_bf16 v[54:57], v[156:159], v[180:183], v[54:57]
	v_mfma_f32_16x16x32_bf16 v[50:53], v[164:167], v[180:183], v[50:53]
	v_mfma_f32_16x16x32_bf16 v[38:41], v[156:159], v[188:191], v[38:41]
	v_mfma_f32_16x16x32_bf16 v[34:37], v[164:167], v[188:191], v[34:37]
	v_mfma_f32_16x16x32_bf16 v[22:25], v[156:159], v[196:199], v[22:25]
	v_mfma_f32_16x16x32_bf16 v[18:21], v[164:167], v[196:199], v[18:21]
	s_setprio 0
	s_barrier
	s_add_u32 s62, s30, 0x80000
	s_addc_u32 s63, s31, 0
	s_add_i32 s61, s48, s37
	s_mov_b32 m0, s61
	s_nop 0
	global_load_lds_dwordx4 v134, s[62:63]
	s_add_i32 m0, s61, 0x2000
	s_nop 0
	global_load_lds_dwordx4 v130, s[62:63]
	s_waitcnt vmcnt(6)
	s_barrier
	s_setprio 1
	v_add_u32_e32 v151, 0x18000, v146
	v_mfma_f32_16x16x32_bf16 v[46:49], v[200:203], v[168:171], v[46:49]
	v_mfma_f32_16x16x32_bf16 v[42:45], v[210:213], v[168:171], v[42:45]
	ds_read_b128 v[152:155], v151
	v_mfma_f32_16x16x32_bf16 v[30:33], v[200:203], v[176:179], v[30:33]
	v_mfma_f32_16x16x32_bf16 v[26:29], v[210:213], v[176:179], v[26:29]
	ds_read_b128 v[156:159], v151 offset:1024
	v_mfma_f32_16x16x32_bf16 v[14:17], v[200:203], v[184:187], v[14:17]
	v_mfma_f32_16x16x32_bf16 v[10:13], v[210:213], v[184:187], v[10:13]
	ds_read_b128 v[160:163], v151 offset:2048
	v_mfma_f32_16x16x32_bf16 v[6:9], v[200:203], v[192:195], v[6:9]
	v_mfma_f32_16x16x32_bf16 v[2:5], v[210:213], v[192:195], v[2:5]
	ds_read_b128 v[164:167], v151 offset:3072
	v_mfma_f32_16x16x32_bf16 v[46:49], v[206:209], v[172:175], v[46:49]
	v_mfma_f32_16x16x32_bf16 v[42:45], v[214:217], v[172:175], v[42:45]
	v_mfma_f32_16x16x32_bf16 v[30:33], v[206:209], v[180:183], v[30:33]
	v_mfma_f32_16x16x32_bf16 v[26:29], v[214:217], v[180:183], v[26:29]
	v_mfma_f32_16x16x32_bf16 v[14:17], v[206:209], v[188:191], v[14:17]
	v_mfma_f32_16x16x32_bf16 v[10:13], v[214:217], v[188:191], v[10:13]
	v_mfma_f32_16x16x32_bf16 v[6:9], v[206:209], v[196:199], v[6:9]
	v_mfma_f32_16x16x32_bf16 v[2:5], v[214:217], v[196:199], v[2:5]
	s_setprio 0
	s_add_i32 s61, 0, 0x18000
	s_barrier
	s_add_u32 s34, s34, 0x80000
	s_addc_u32 s35, s35, 0
	s_mov_b32 m0, s41
	ds_read_b128 v[168:171], v149 offset:32768
	ds_read_b128 v[172:175], v149 offset:33792
	ds_read_b128 v[176:179], v149 offset:34816
	ds_read_b128 v[180:183], v149 offset:35840
	ds_read_b128 v[184:187], v149 offset:36864
	ds_read_b128 v[188:191], v149 offset:37888
	ds_read_b128 v[192:195], v149 offset:38912
	ds_read_b128 v[196:199], v149 offset:39936
	global_load_lds_dwordx4 v136, s[34:35]
	s_mov_b32 m0, s42
	s_nop 0
	global_load_lds_dwordx4 v132, s[34:35]
	s_barrier
	s_waitcnt lgkmcnt(0)
	s_setprio 1
	v_add_u32_e32 v151, 0x1c000, v146
	s_waitcnt lgkmcnt(0)
	v_mfma_f32_16x16x32_bf16 v[126:129], v[152:155], v[168:171], v[126:129]
	v_mfma_f32_16x16x32_bf16 v[122:125], v[160:163], v[168:171], v[122:125]
	ds_read_b128 v[200:203], v151
	v_mfma_f32_16x16x32_bf16 v[118:121], v[152:155], v[176:179], v[118:121]
	v_mfma_f32_16x16x32_bf16 v[114:117], v[160:163], v[176:179], v[114:117]
	ds_read_b128 v[206:209], v151 offset:1024
	v_mfma_f32_16x16x32_bf16 v[102:105], v[152:155], v[184:187], v[102:105]
	v_mfma_f32_16x16x32_bf16 v[98:101], v[160:163], v[184:187], v[98:101]
	ds_read_b128 v[210:213], v151 offset:2048
	v_mfma_f32_16x16x32_bf16 v[86:89], v[152:155], v[192:195], v[86:89]
	v_mfma_f32_16x16x32_bf16 v[82:85], v[160:163], v[192:195], v[82:85]
	ds_read_b128 v[214:217], v151 offset:3072
	v_mfma_f32_16x16x32_bf16 v[126:129], v[156:159], v[172:175], v[126:129]
	v_mfma_f32_16x16x32_bf16 v[122:125], v[164:167], v[172:175], v[122:125]
	v_mfma_f32_16x16x32_bf16 v[118:121], v[156:159], v[180:183], v[118:121]
	v_mfma_f32_16x16x32_bf16 v[114:117], v[164:167], v[180:183], v[114:117]
	v_mfma_f32_16x16x32_bf16 v[102:105], v[156:159], v[188:191], v[102:105]
	v_mfma_f32_16x16x32_bf16 v[98:101], v[164:167], v[188:191], v[98:101]
	v_mfma_f32_16x16x32_bf16 v[86:89], v[156:159], v[196:199], v[86:89]
	v_mfma_f32_16x16x32_bf16 v[82:85], v[164:167], v[196:199], v[82:85]
	s_setprio 0
	s_barrier
	s_add_i32 s34, 0, 0x1c000
	s_add_i32 s35, s61, s37
	s_mov_b32 m0, s35
	global_load_lds_dwordx4 v134, s[66:67]
	s_add_i32 m0, s35, 0x2000
	s_nop 0
	global_load_lds_dwordx4 v130, s[66:67]
	s_barrier
	s_waitcnt lgkmcnt(0)
	s_setprio 1
	s_waitcnt lgkmcnt(0)
	v_mfma_f32_16x16x32_bf16 v[110:113], v[200:203], v[168:171], v[110:113]
	v_mfma_f32_16x16x32_bf16 v[106:109], v[210:213], v[168:171], v[106:109]
	v_mfma_f32_16x16x32_bf16 v[94:97], v[200:203], v[176:179], v[94:97]
	v_mfma_f32_16x16x32_bf16 v[90:93], v[210:213], v[176:179], v[90:93]
	v_mfma_f32_16x16x32_bf16 v[78:81], v[200:203], v[184:187], v[78:81]
	v_mfma_f32_16x16x32_bf16 v[74:77], v[210:213], v[184:187], v[74:77]
	v_mfma_f32_16x16x32_bf16 v[70:73], v[200:203], v[192:195], v[70:73]
	v_mfma_f32_16x16x32_bf16 v[66:69], v[210:213], v[192:195], v[66:69]
	v_mfma_f32_16x16x32_bf16 v[110:113], v[206:209], v[172:175], v[110:113]
	v_mfma_f32_16x16x32_bf16 v[106:109], v[214:217], v[172:175], v[106:109]
	v_mfma_f32_16x16x32_bf16 v[94:97], v[206:209], v[180:183], v[94:97]
	v_mfma_f32_16x16x32_bf16 v[90:93], v[214:217], v[180:183], v[90:93]
	v_mfma_f32_16x16x32_bf16 v[78:81], v[206:209], v[188:191], v[78:81]
	v_mfma_f32_16x16x32_bf16 v[74:77], v[214:217], v[188:191], v[74:77]
	v_mfma_f32_16x16x32_bf16 v[70:73], v[206:209], v[196:199], v[70:73]
	v_mfma_f32_16x16x32_bf16 v[66:69], v[214:217], v[196:199], v[66:69]
	s_setprio 0
	s_mov_b32 m0, s44
	s_barrier
	ds_read_b128 v[168:171], v149 offset:49152
	ds_read_b128 v[172:175], v149 offset:50176
	ds_read_b128 v[176:179], v149 offset:51200
	ds_read_b128 v[180:183], v149 offset:52224
	ds_read_b128 v[184:187], v149 offset:53248
	ds_read_b128 v[188:191], v149 offset:54272
	ds_read_b128 v[192:195], v149 offset:55296
	ds_read_b128 v[196:199], v149 offset:56320
	global_load_lds_dwordx4 v136, s[68:69]
	s_mov_b32 m0, s45
	s_nop 0
	global_load_lds_dwordx4 v132, s[68:69]
	s_waitcnt vmcnt(8)
	s_barrier
	s_waitcnt lgkmcnt(0)
	s_setprio 1
	s_waitcnt lgkmcnt(0)
	v_mfma_f32_16x16x32_bf16 v[62:65], v[152:155], v[168:171], v[62:65]
	v_mfma_f32_16x16x32_bf16 v[58:61], v[160:163], v[168:171], v[58:61]
	v_mfma_f32_16x16x32_bf16 v[54:57], v[152:155], v[176:179], v[54:57]
	v_mfma_f32_16x16x32_bf16 v[50:53], v[160:163], v[176:179], v[50:53]
	v_mfma_f32_16x16x32_bf16 v[38:41], v[152:155], v[184:187], v[38:41]
	v_mfma_f32_16x16x32_bf16 v[34:37], v[160:163], v[184:187], v[34:37]
	v_mfma_f32_16x16x32_bf16 v[22:25], v[152:155], v[192:195], v[22:25]
	v_mfma_f32_16x16x32_bf16 v[18:21], v[160:163], v[192:195], v[18:21]
	v_mfma_f32_16x16x32_bf16 v[62:65], v[156:159], v[172:175], v[62:65]
	v_mfma_f32_16x16x32_bf16 v[58:61], v[164:167], v[172:175], v[58:61]
	v_mfma_f32_16x16x32_bf16 v[54:57], v[156:159], v[180:183], v[54:57]
	v_mfma_f32_16x16x32_bf16 v[50:53], v[164:167], v[180:183], v[50:53]
	v_mfma_f32_16x16x32_bf16 v[38:41], v[156:159], v[188:191], v[38:41]
	v_mfma_f32_16x16x32_bf16 v[34:37], v[164:167], v[188:191], v[34:37]
	v_mfma_f32_16x16x32_bf16 v[22:25], v[156:159], v[196:199], v[22:25]
	v_mfma_f32_16x16x32_bf16 v[18:21], v[164:167], v[196:199], v[18:21]
	s_setprio 0
	s_barrier
	s_add_u32 s30, s30, 0x80080
	s_addc_u32 s31, s31, 0
	s_add_i32 s34, s34, s37
	s_mov_b32 m0, s34
	s_nop 0
	global_load_lds_dwordx4 v134, s[30:31]
	s_add_i32 m0, s34, 0x2000
	s_nop 0
	global_load_lds_dwordx4 v130, s[30:31]
	s_waitcnt vmcnt(6)
	s_barrier
	s_setprio 1
	v_mfma_f32_16x16x32_bf16 v[46:49], v[200:203], v[168:171], v[46:49]
	v_mfma_f32_16x16x32_bf16 v[42:45], v[210:213], v[168:171], v[42:45]
	ds_read_b128 v[152:155], v148
	v_mfma_f32_16x16x32_bf16 v[30:33], v[200:203], v[176:179], v[30:33]
	v_mfma_f32_16x16x32_bf16 v[26:29], v[210:213], v[176:179], v[26:29]
	ds_read_b128 v[156:159], v148 offset:1024
	v_mfma_f32_16x16x32_bf16 v[14:17], v[200:203], v[184:187], v[14:17]
	v_mfma_f32_16x16x32_bf16 v[10:13], v[210:213], v[184:187], v[10:13]
	ds_read_b128 v[160:163], v148 offset:2048
	v_mfma_f32_16x16x32_bf16 v[6:9], v[200:203], v[192:195], v[6:9]
	v_mfma_f32_16x16x32_bf16 v[2:5], v[210:213], v[192:195], v[2:5]
	ds_read_b128 v[164:167], v148 offset:3072
	v_mfma_f32_16x16x32_bf16 v[46:49], v[206:209], v[172:175], v[46:49]
	v_mfma_f32_16x16x32_bf16 v[42:45], v[214:217], v[172:175], v[42:45]
	v_mfma_f32_16x16x32_bf16 v[30:33], v[206:209], v[180:183], v[30:33]
	v_mfma_f32_16x16x32_bf16 v[26:29], v[214:217], v[180:183], v[26:29]
	v_mfma_f32_16x16x32_bf16 v[14:17], v[206:209], v[188:191], v[14:17]
	v_mfma_f32_16x16x32_bf16 v[10:13], v[214:217], v[188:191], v[10:13]
	v_mfma_f32_16x16x32_bf16 v[6:9], v[206:209], v[196:199], v[6:9]
	v_mfma_f32_16x16x32_bf16 v[2:5], v[214:217], v[196:199], v[2:5]
	s_setprio 0
	s_add_i32 s60, s60, 2
	s_add_u32 s28, s28, 0x100
	s_addc_u32 s29, s29, 0
	s_add_u32 s56, s56, 0x100
	s_addc_u32 s57, s57, 0
	s_cmp_gt_u32 s60, 29
	s_barrier
	s_cbranch_scc0 .LBB0_620
	s_waitcnt lgkmcnt(0)
	v_lshl_add_u32 v152, s16, 8, v1
	v_lshl_or_b32 v154, s53, 8, v147
	v_ashrrev_i32_e32 v153, 31, v152
	v_ashrrev_i32_e32 v155, 31, v154
	v_lshlrev_b64 v[156:157], 12, v[152:153]
	v_lshl_add_u64 v[156:157], s[96:97], 0, v[156:157]
	v_lshlrev_b64 v[154:155], 1, v[154:155]
	v_lshl_add_u64 v[156:157], v[156:157], 0, v[154:155]
	v_cvt_pk_bf16_f32 v62, v62, v63
	v_cvt_pk_bf16_f32 v63, v64, v65
	v_cvt_pk_bf16_f32 v64, v58, v59
	v_add_co_u32_e32 v58, vcc, s49, v156
	v_cvt_pk_bf16_f32 v70, v70, v71
	v_cvt_pk_bf16_f32 v71, v72, v73
	v_cvt_pk_bf16_f32 v72, v66, v67
	v_lshl_add_u64 v[66:67], v[156:157], 0, s[6:7]
	v_addc_co_u32_e32 v59, vcc, 0, v157, vcc
	v_cvt_pk_bf16_f32 v46, v46, v47
	v_cvt_pk_bf16_f32 v47, v48, v49
	v_cvt_pk_bf16_f32 v48, v42, v43
	v_cvt_pk_bf16_f32 v49, v44, v45
	v_cvt_pk_bf16_f32 v110, v110, v111
	v_cvt_pk_bf16_f32 v111, v112, v113
	v_cvt_pk_bf16_f32 v112, v106, v107
	v_or_b32_e32 v106, 16, v152
	global_store_dwordx4 v[66:67], v[46:49], off offset:256
	v_ashrrev_i32_e32 v107, 31, v106
	v_cvt_pk_bf16_f32 v94, v94, v95
	v_add_co_u32_e32 v48, vcc, s50, v156
	v_cvt_pk_bf16_f32 v95, v96, v97
	v_cvt_pk_bf16_f32 v96, v90, v91
	v_or_b32_e32 v90, 32, v152
	v_lshl_add_u64 v[46:47], v[156:157], 0, s[10:11]
	v_addc_co_u32_e32 v49, vcc, 0, v157, vcc
	v_cvt_pk_bf16_f32 v30, v30, v31
	v_cvt_pk_bf16_f32 v31, v32, v33
	v_cvt_pk_bf16_f32 v32, v26, v27
	v_cvt_pk_bf16_f32 v33, v28, v29
	v_lshlrev_b64 v[106:107], 12, v[106:107]
	v_ashrrev_i32_e32 v91, 31, v90
	v_cvt_pk_bf16_f32 v78, v78, v79
	v_cvt_pk_bf16_f32 v79, v80, v81
	v_cvt_pk_bf16_f32 v80, v74, v75
	v_or_b32_e32 v74, 48, v152
	global_store_dwordx4 v[46:47], v[30:33], off offset:256
	v_cvt_pk_bf16_f32 v113, v108, v109
	v_lshl_add_u64 v[106:107], s[96:97], 0, v[106:107]
	v_add_co_u32_e32 v32, vcc, s51, v156
	v_lshlrev_b64 v[90:91], 12, v[90:91]
	v_ashrrev_i32_e32 v75, 31, v74
	v_lshl_add_u64 v[30:31], v[156:157], 0, s[12:13]
	v_addc_co_u32_e32 v33, vcc, 0, v157, vcc
	v_cvt_pk_bf16_f32 v14, v14, v15
	v_cvt_pk_bf16_f32 v15, v16, v17
	v_cvt_pk_bf16_f32 v16, v10, v11
	v_cvt_pk_bf16_f32 v17, v12, v13
	global_store_dwordx4 v[156:157], v[110:113], off offset:256
	v_cvt_pk_bf16_f32 v97, v92, v93
	v_lshl_add_u64 v[90:91], s[96:97], 0, v[90:91]
	v_lshl_add_u64 v[110:111], v[106:107], 0, v[154:155]
	v_lshlrev_b64 v[74:75], 12, v[74:75]
	global_store_dwordx4 v[30:31], v[14:17], off offset:256
	global_store_dwordx4 v[110:111], v[94:97], off offset:256
	v_cvt_pk_bf16_f32 v81, v76, v77
	v_add_co_u32_e32 v16, vcc, s52, v156
	v_lshl_add_u64 v[94:95], v[90:91], 0, v[154:155]
	v_lshl_add_u64 v[74:75], s[96:97], 0, v[74:75]
	v_addc_co_u32_e32 v17, vcc, 0, v157, vcc
	v_cvt_pk_bf16_f32 v126, v126, v127
	v_cvt_pk_bf16_f32 v127, v128, v129
	v_cvt_pk_bf16_f32 v128, v122, v123
	v_cvt_pk_bf16_f32 v129, v124, v125
	v_cvt_pk_bf16_f32 v106, v118, v119
	v_cvt_pk_bf16_f32 v107, v120, v121
	v_cvt_pk_bf16_f32 v108, v114, v115
	v_cvt_pk_bf16_f32 v109, v116, v117
	v_cvt_pk_bf16_f32 v90, v102, v103
	v_cvt_pk_bf16_f32 v91, v104, v105
	v_cvt_pk_bf16_f32 v92, v98, v99
	v_cvt_pk_bf16_f32 v93, v100, v101
	global_store_dwordx4 v[94:95], v[78:81], off offset:256
	v_cvt_pk_bf16_f32 v76, v82, v83
	v_cvt_pk_bf16_f32 v77, v84, v85
	v_lshl_add_u64 v[78:79], v[74:75], 0, v[154:155]
	v_cvt_pk_bf16_f32 v74, v86, v87
	v_cvt_pk_bf16_f32 v75, v88, v89
	v_cvt_pk_bf16_f32 v73, v68, v69
	v_cvt_pk_bf16_f32 v65, v60, v61
	v_cvt_pk_bf16_f32 v42, v54, v55
	v_cvt_pk_bf16_f32 v43, v56, v57
	v_cvt_pk_bf16_f32 v44, v50, v51
	v_cvt_pk_bf16_f32 v45, v52, v53
	v_cvt_pk_bf16_f32 v26, v38, v39
	v_cvt_pk_bf16_f32 v27, v40, v41
	v_cvt_pk_bf16_f32 v28, v34, v35
	v_cvt_pk_bf16_f32 v29, v36, v37
	v_lshl_add_u64 v[14:15], v[156:157], 0, s[14:15]
	v_cvt_pk_bf16_f32 v10, v22, v23
	v_cvt_pk_bf16_f32 v11, v24, v25
	v_cvt_pk_bf16_f32 v12, v18, v19
	v_cvt_pk_bf16_f32 v13, v20, v21
	v_cvt_pk_bf16_f32 v6, v6, v7
	v_cvt_pk_bf16_f32 v7, v8, v9
	v_cvt_pk_bf16_f32 v8, v2, v3
	v_cvt_pk_bf16_f32 v9, v4, v5
	s_and_b64 vcc, exec, s[0:1]
	s_mov_b32 s53, s18
	s_mov_b32 s16, s20
	s_mov_b64 s[30:31], s[26:27]
	s_mov_b64 s[28:29], s[22:23]
	global_store_dwordx4 v[156:157], v[126:129], off
	global_store_dwordx4 v[110:111], v[106:109], off
	global_store_dwordx4 v[94:95], v[90:93], off
	global_store_dwordx4 v[78:79], v[74:77], off
	global_store_dwordx4 v[78:79], v[70:73], off offset:256
	global_store_dwordx4 v[58:59], v[62:65], off
	global_store_dwordx4 v[48:49], v[42:45], off
	global_store_dwordx4 v[32:33], v[26:29], off
	global_store_dwordx4 v[16:17], v[10:13], off
	global_store_dwordx4 v[14:15], v[6:9], off offset:256
	s_cbranch_vccz .LBB0_617
	s_waitcnt vmcnt(0)
	s_cmpk_gt_u32 s2, 0xff
	s_cbranch_scc1 .LBB0_624
	s_barrier

.LBB0_1368:
	s_ashr_i32 s21, s20, 31
	v_cmp_lt_i64_e32 vcc, s[22:23], v[142:143]
	s_lshl_b64 s[22:23], s[20:21], 20
	v_readlane_b32 s19, v254, 36
	s_add_u32 s22, s19, s22
	v_readlane_b32 s19, v254, 37
	s_addc_u32 s23, s19, s23
	s_and_b64 s[24:25], vcc, exec
	s_cselect_b32 s21, s23, s27
	s_cselect_b32 s50, s22, s26
	s_ashr_i32 s19, s18, 31
	s_lshl_b64 s[24:25], s[18:19], 20
	s_add_u32 s24, s33, s24
	s_addc_u32 s25, s34, s25
	s_and_b64 s[30:31], vcc, exec
	s_cselect_b32 s19, s25, s29
	s_cselect_b32 s51, s24, s28
	s_add_u32 s26, s26, 0x80080
	s_addc_u32 s27, s27, 0
	s_add_u32 s52, s28, 0x100
	v_mov_b32_e32 v2, 0
	s_addc_u32 s53, s29, 0
	s_mov_b32 s54, -2
	v_mov_b32_e32 v3, v2
	v_mov_b32_e32 v4, v2
	v_mov_b32_e32 v5, v2
	v_mov_b32_e32 v6, v2
	v_mov_b32_e32 v7, v2
	v_mov_b32_e32 v8, v2
	v_mov_b32_e32 v9, v2
	v_mov_b32_e32 v10, v2
	v_mov_b32_e32 v11, v2
	v_mov_b32_e32 v12, v2
	v_mov_b32_e32 v13, v2
	v_mov_b32_e32 v14, v2
	v_mov_b32_e32 v15, v2
	v_mov_b32_e32 v16, v2
	v_mov_b32_e32 v17, v2
	v_mov_b32_e32 v26, v2
	v_mov_b32_e32 v27, v2
	v_mov_b32_e32 v28, v2
	v_mov_b32_e32 v29, v2
	v_mov_b32_e32 v30, v2
	v_mov_b32_e32 v31, v2
	v_mov_b32_e32 v32, v2
	v_mov_b32_e32 v33, v2
	v_mov_b32_e32 v42, v2
	v_mov_b32_e32 v43, v2
	v_mov_b32_e32 v44, v2
	v_mov_b32_e32 v45, v2
	v_mov_b32_e32 v46, v2
	v_mov_b32_e32 v47, v2
	v_mov_b32_e32 v48, v2
	v_mov_b32_e32 v49, v2
	v_mov_b32_e32 v18, v2
	v_mov_b32_e32 v19, v2
	v_mov_b32_e32 v20, v2
	v_mov_b32_e32 v21, v2
	v_mov_b32_e32 v22, v2
	v_mov_b32_e32 v23, v2
	v_mov_b32_e32 v24, v2
	v_mov_b32_e32 v25, v2
	v_mov_b32_e32 v34, v2
	v_mov_b32_e32 v35, v2
	v_mov_b32_e32 v36, v2
	v_mov_b32_e32 v37, v2
	v_mov_b32_e32 v38, v2
	v_mov_b32_e32 v39, v2
	v_mov_b32_e32 v40, v2
	v_mov_b32_e32 v41, v2
	v_mov_b32_e32 v50, v2
	v_mov_b32_e32 v51, v2
	v_mov_b32_e32 v52, v2
	v_mov_b32_e32 v53, v2
	v_mov_b32_e32 v54, v2
	v_mov_b32_e32 v55, v2
	v_mov_b32_e32 v56, v2
	v_mov_b32_e32 v57, v2
	v_mov_b32_e32 v58, v2
	v_mov_b32_e32 v59, v2
	v_mov_b32_e32 v60, v2
	v_mov_b32_e32 v61, v2
	v_mov_b32_e32 v62, v2
	v_mov_b32_e32 v63, v2
	v_mov_b32_e32 v64, v2
	v_mov_b32_e32 v65, v2
	v_mov_b32_e32 v66, v2
	v_mov_b32_e32 v67, v2
	v_mov_b32_e32 v68, v2
	v_mov_b32_e32 v69, v2
	v_mov_b32_e32 v70, v2
	v_mov_b32_e32 v71, v2
	v_mov_b32_e32 v72, v2
	v_mov_b32_e32 v73, v2
	v_mov_b32_e32 v74, v2
	v_mov_b32_e32 v75, v2
	v_mov_b32_e32 v76, v2
	v_mov_b32_e32 v77, v2
	v_mov_b32_e32 v78, v2
	v_mov_b32_e32 v79, v2
	v_mov_b32_e32 v80, v2
	v_mov_b32_e32 v81, v2
	v_mov_b32_e32 v90, v2
	v_mov_b32_e32 v91, v2
	v_mov_b32_e32 v92, v2
	v_mov_b32_e32 v93, v2
	v_mov_b32_e32 v94, v2
	v_mov_b32_e32 v95, v2
	v_mov_b32_e32 v96, v2
	v_mov_b32_e32 v97, v2
	v_mov_b32_e32 v106, v2
	v_mov_b32_e32 v107, v2
	v_mov_b32_e32 v108, v2
	v_mov_b32_e32 v109, v2
	v_mov_b32_e32 v110, v2
	v_mov_b32_e32 v111, v2
	v_mov_b32_e32 v112, v2
	v_mov_b32_e32 v113, v2
	v_mov_b32_e32 v82, v2
	v_mov_b32_e32 v83, v2
	v_mov_b32_e32 v84, v2
	v_mov_b32_e32 v85, v2
	v_mov_b32_e32 v86, v2
	v_mov_b32_e32 v87, v2
	v_mov_b32_e32 v88, v2
	v_mov_b32_e32 v89, v2
	v_mov_b32_e32 v98, v2
	v_mov_b32_e32 v99, v2
	v_mov_b32_e32 v100, v2
	v_mov_b32_e32 v101, v2
	v_mov_b32_e32 v102, v2
	v_mov_b32_e32 v103, v2
	v_mov_b32_e32 v104, v2
	v_mov_b32_e32 v105, v2
	v_mov_b32_e32 v114, v2
	v_mov_b32_e32 v115, v2
	v_mov_b32_e32 v116, v2
	v_mov_b32_e32 v117, v2
	v_mov_b32_e32 v118, v2
	v_mov_b32_e32 v119, v2
	v_mov_b32_e32 v120, v2
	v_mov_b32_e32 v121, v2
	v_mov_b32_e32 v122, v2
	v_mov_b32_e32 v123, v2
	v_mov_b32_e32 v124, v2
	v_mov_b32_e32 v125, v2
	v_mov_b32_e32 v126, v2
	v_mov_b32_e32 v127, v2
	v_mov_b32_e32 v128, v2
	v_mov_b32_e32 v129, v2
	ds_read_b128 v[152:155], v149
	ds_read_b128 v[156:159], v149 offset:1024
	ds_read_b128 v[160:163], v149 offset:2048
	ds_read_b128 v[164:167], v149 offset:3072
.LBB0_1369:
	s_add_u32 s28, s26, 0xfff80080
	s_addc_u32 s29, s27, -1
	s_cmp_eq_u32 s54, 28
	s_cselect_b32 s31, s21, s29
	s_cselect_b32 s30, s50, s28
	s_cselect_b32 s29, s19, s53
	s_cselect_b32 s28, s51, s52
	s_add_i32 m0, s17, 0xc000
	ds_read_b128 v[168:171], v150
	ds_read_b128 v[172:175], v150 offset:1024
	ds_read_b128 v[176:179], v150 offset:2048
	ds_read_b128 v[180:183], v150 offset:3072
	ds_read_b128 v[184:187], v150 offset:4096
	ds_read_b128 v[190:193], v150 offset:5120
	ds_read_b128 v[194:197], v150 offset:6144
	ds_read_b128 v[198:201], v150 offset:7168
	global_load_lds_dwordx4 v138, s[26:27]
	s_add_i32 m0, s17, 0xe000
	s_nop 0
	global_load_lds_dwordx4 v140, s[26:27]
	s_barrier
	s_waitcnt lgkmcnt(0)
	s_setprio 1
	s_waitcnt lgkmcnt(0)
	v_mfma_f32_16x16x32_bf16 v[126:129], v[152:155], v[168:171], v[126:129]
	v_mfma_f32_16x16x32_bf16 v[122:125], v[160:163], v[168:171], v[122:125]
	ds_read_b128 v[214:217], v151
	v_mfma_f32_16x16x32_bf16 v[118:121], v[152:155], v[176:179], v[118:121]
	v_mfma_f32_16x16x32_bf16 v[114:117], v[160:163], v[176:179], v[114:117]
	ds_read_b128 v[218:221], v151 offset:1024
	v_mfma_f32_16x16x32_bf16 v[102:105], v[152:155], v[184:187], v[102:105]
	v_mfma_f32_16x16x32_bf16 v[98:101], v[160:163], v[184:187], v[98:101]
	ds_read_b128 v[222:225], v151 offset:2048
	v_mfma_f32_16x16x32_bf16 v[86:89], v[152:155], v[194:197], v[86:89]
	v_mfma_f32_16x16x32_bf16 v[82:85], v[160:163], v[194:197], v[82:85]
	ds_read_b128 v[226:229], v151 offset:3072
	v_mfma_f32_16x16x32_bf16 v[126:129], v[156:159], v[172:175], v[126:129]
	v_mfma_f32_16x16x32_bf16 v[122:125], v[164:167], v[172:175], v[122:125]
	v_mfma_f32_16x16x32_bf16 v[118:121], v[156:159], v[180:183], v[118:121]
	v_mfma_f32_16x16x32_bf16 v[114:117], v[164:167], v[180:183], v[114:117]
	v_mfma_f32_16x16x32_bf16 v[102:105], v[156:159], v[190:193], v[102:105]
	v_mfma_f32_16x16x32_bf16 v[98:101], v[164:167], v[190:193], v[98:101]
	v_mfma_f32_16x16x32_bf16 v[86:89], v[156:159], v[198:201], v[86:89]
	v_mfma_f32_16x16x32_bf16 v[82:85], v[164:167], v[198:201], v[82:85]
	s_setprio 0
	s_barrier
	s_add_i32 s55, s43, s35
	s_add_u32 s66, s28, 0x80
	s_addc_u32 s67, s29, 0
	s_mov_b32 m0, s55
	global_load_lds_dwordx4 v132, s[28:29]
	s_add_i32 m0, s55, 0x2000
	s_nop 0
	global_load_lds_dwordx4 v136, s[28:29]
	s_barrier
	s_waitcnt lgkmcnt(0)
	s_setprio 1
	s_waitcnt lgkmcnt(0)
	v_mfma_f32_16x16x32_bf16 v[110:113], v[214:217], v[168:171], v[110:113]
	v_mfma_f32_16x16x32_bf16 v[106:109], v[222:225], v[168:171], v[106:109]
	v_mfma_f32_16x16x32_bf16 v[94:97], v[214:217], v[176:179], v[94:97]
	v_mfma_f32_16x16x32_bf16 v[90:93], v[222:225], v[176:179], v[90:93]
	v_mfma_f32_16x16x32_bf16 v[78:81], v[214:217], v[184:187], v[78:81]
	v_mfma_f32_16x16x32_bf16 v[74:77], v[222:225], v[184:187], v[74:77]
	v_mfma_f32_16x16x32_bf16 v[70:73], v[214:217], v[194:197], v[70:73]
	v_mfma_f32_16x16x32_bf16 v[66:69], v[222:225], v[194:197], v[66:69]
	v_mfma_f32_16x16x32_bf16 v[110:113], v[218:221], v[172:175], v[110:113]
	v_mfma_f32_16x16x32_bf16 v[106:109], v[226:229], v[172:175], v[106:109]
	v_mfma_f32_16x16x32_bf16 v[94:97], v[218:221], v[180:183], v[94:97]
	v_mfma_f32_16x16x32_bf16 v[90:93], v[226:229], v[180:183], v[90:93]
	v_mfma_f32_16x16x32_bf16 v[78:81], v[218:221], v[190:193], v[78:81]
	v_mfma_f32_16x16x32_bf16 v[74:77], v[226:229], v[190:193], v[74:77]
	v_mfma_f32_16x16x32_bf16 v[70:73], v[218:221], v[198:201], v[70:73]
	v_mfma_f32_16x16x32_bf16 v[66:69], v[226:229], v[198:201], v[66:69]
	s_setprio 0
	s_mov_b32 m0, s17
	s_add_u32 s68, s30, 0x80
	s_addc_u32 s69, s31, 0
	s_barrier
	ds_read_b128 v[168:171], v150 offset:16384
	ds_read_b128 v[172:175], v150 offset:17408
	ds_read_b128 v[176:179], v150 offset:18432
	ds_read_b128 v[180:183], v150 offset:19456
	ds_read_b128 v[184:187], v150 offset:20480
	ds_read_b128 v[190:193], v150 offset:21504
	ds_read_b128 v[194:197], v150 offset:22528
	ds_read_b128 v[198:201], v150 offset:23552
	global_load_lds_dwordx4 v130, s[30:31]
	s_mov_b32 m0, s36
	s_nop 0
	global_load_lds_dwordx4 v134, s[30:31]
	s_waitcnt vmcnt(8)
	s_barrier
	s_waitcnt lgkmcnt(0)
	s_setprio 1
	s_waitcnt lgkmcnt(0)
	v_mfma_f32_16x16x32_bf16 v[62:65], v[152:155], v[168:171], v[62:65]
	v_mfma_f32_16x16x32_bf16 v[58:61], v[160:163], v[168:171], v[58:61]
	v_mfma_f32_16x16x32_bf16 v[54:57], v[152:155], v[176:179], v[54:57]
	v_mfma_f32_16x16x32_bf16 v[50:53], v[160:163], v[176:179], v[50:53]
	v_mfma_f32_16x16x32_bf16 v[38:41], v[152:155], v[184:187], v[38:41]
	v_mfma_f32_16x16x32_bf16 v[34:37], v[160:163], v[184:187], v[34:37]
	v_mfma_f32_16x16x32_bf16 v[22:25], v[152:155], v[194:197], v[22:25]
	v_mfma_f32_16x16x32_bf16 v[18:21], v[160:163], v[194:197], v[18:21]
	v_mfma_f32_16x16x32_bf16 v[62:65], v[156:159], v[172:175], v[62:65]
	v_mfma_f32_16x16x32_bf16 v[58:61], v[164:167], v[172:175], v[58:61]
	v_mfma_f32_16x16x32_bf16 v[54:57], v[156:159], v[180:183], v[54:57]
	v_mfma_f32_16x16x32_bf16 v[50:53], v[164:167], v[180:183], v[50:53]
	v_mfma_f32_16x16x32_bf16 v[38:41], v[156:159], v[190:193], v[38:41]
	v_mfma_f32_16x16x32_bf16 v[34:37], v[164:167], v[190:193], v[34:37]
	v_mfma_f32_16x16x32_bf16 v[22:25], v[156:159], v[198:201], v[22:25]
	v_mfma_f32_16x16x32_bf16 v[18:21], v[164:167], v[198:201], v[18:21]
	s_setprio 0
	s_barrier
	s_add_u32 s56, s28, 0x80000
	s_addc_u32 s57, s29, 0
	s_add_i32 s55, s44, s35
	s_mov_b32 m0, s55
	s_nop 0
	global_load_lds_dwordx4 v132, s[56:57]
	s_add_i32 m0, s55, 0x2000
	s_nop 0
	global_load_lds_dwordx4 v136, s[56:57]
	s_waitcnt vmcnt(6)
	s_barrier
	s_setprio 1
	v_add_u32_e32 v164, 0x18000, v147
	v_mfma_f32_16x16x32_bf16 v[46:49], v[214:217], v[168:171], v[46:49]
	v_mfma_f32_16x16x32_bf16 v[42:45], v[222:225], v[168:171], v[42:45]
	ds_read_b128 v[152:155], v164
	v_mfma_f32_16x16x32_bf16 v[30:33], v[214:217], v[176:179], v[30:33]
	v_mfma_f32_16x16x32_bf16 v[26:29], v[222:225], v[176:179], v[26:29]
	ds_read_b128 v[156:159], v164 offset:1024
	v_mfma_f32_16x16x32_bf16 v[14:17], v[214:217], v[184:187], v[14:17]
	v_mfma_f32_16x16x32_bf16 v[10:13], v[222:225], v[184:187], v[10:13]
	ds_read_b128 v[160:163], v164 offset:2048
	v_mfma_f32_16x16x32_bf16 v[6:9], v[214:217], v[194:197], v[6:9]
	v_mfma_f32_16x16x32_bf16 v[2:5], v[222:225], v[194:197], v[2:5]
	ds_read_b128 v[164:167], v164 offset:3072
	v_mfma_f32_16x16x32_bf16 v[46:49], v[218:221], v[172:175], v[46:49]
	v_mfma_f32_16x16x32_bf16 v[42:45], v[226:229], v[172:175], v[42:45]
	v_mfma_f32_16x16x32_bf16 v[30:33], v[218:221], v[180:183], v[30:33]
	v_mfma_f32_16x16x32_bf16 v[26:29], v[226:229], v[180:183], v[26:29]
	v_mfma_f32_16x16x32_bf16 v[14:17], v[218:221], v[190:193], v[14:17]
	v_mfma_f32_16x16x32_bf16 v[10:13], v[226:229], v[190:193], v[10:13]
	v_mfma_f32_16x16x32_bf16 v[6:9], v[218:221], v[198:201], v[6:9]
	v_mfma_f32_16x16x32_bf16 v[2:5], v[226:229], v[198:201], v[2:5]
	s_setprio 0
	s_add_i32 s55, 0, 0x18000
	s_barrier
	s_add_u32 s30, s30, 0x80000
	s_addc_u32 s31, s31, 0
	s_mov_b32 m0, s37
	ds_read_b128 v[168:171], v150 offset:32768
	ds_read_b128 v[172:175], v150 offset:33792
	ds_read_b128 v[176:179], v150 offset:34816
	ds_read_b128 v[180:183], v150 offset:35840
	ds_read_b128 v[184:187], v150 offset:36864
	ds_read_b128 v[190:193], v150 offset:37888
	ds_read_b128 v[194:197], v150 offset:38912
	ds_read_b128 v[198:201], v150 offset:39936
	global_load_lds_dwordx4 v130, s[30:31]
	s_mov_b32 m0, s38
	s_nop 0
	global_load_lds_dwordx4 v134, s[30:31]
	s_barrier
	s_waitcnt lgkmcnt(0)
	s_setprio 1
	v_add_u32_e32 v213, 0x1c000, v147
	s_waitcnt lgkmcnt(0)
	v_mfma_f32_16x16x32_bf16 v[126:129], v[152:155], v[168:171], v[126:129]
	v_mfma_f32_16x16x32_bf16 v[122:125], v[160:163], v[168:171], v[122:125]
	ds_read_b128 v[214:217], v213
	v_mfma_f32_16x16x32_bf16 v[118:121], v[152:155], v[176:179], v[118:121]
	v_mfma_f32_16x16x32_bf16 v[114:117], v[160:163], v[176:179], v[114:117]
	ds_read_b128 v[218:221], v213 offset:1024
	v_mfma_f32_16x16x32_bf16 v[102:105], v[152:155], v[184:187], v[102:105]
	v_mfma_f32_16x16x32_bf16 v[98:101], v[160:163], v[184:187], v[98:101]
	ds_read_b128 v[222:225], v213 offset:2048
	v_mfma_f32_16x16x32_bf16 v[86:89], v[152:155], v[194:197], v[86:89]
	v_mfma_f32_16x16x32_bf16 v[82:85], v[160:163], v[194:197], v[82:85]
	ds_read_b128 v[226:229], v213 offset:3072
	v_mfma_f32_16x16x32_bf16 v[126:129], v[156:159], v[172:175], v[126:129]
	v_mfma_f32_16x16x32_bf16 v[122:125], v[164:167], v[172:175], v[122:125]
	v_mfma_f32_16x16x32_bf16 v[118:121], v[156:159], v[180:183], v[118:121]
	v_mfma_f32_16x16x32_bf16 v[114:117], v[164:167], v[180:183], v[114:117]
	v_mfma_f32_16x16x32_bf16 v[102:105], v[156:159], v[190:193], v[102:105]
	v_mfma_f32_16x16x32_bf16 v[98:101], v[164:167], v[190:193], v[98:101]
	v_mfma_f32_16x16x32_bf16 v[86:89], v[156:159], v[198:201], v[86:89]
	v_mfma_f32_16x16x32_bf16 v[82:85], v[164:167], v[198:201], v[82:85]
	s_setprio 0
	s_barrier
	s_add_i32 s30, 0, 0x1c000
	s_add_i32 s31, s55, s35
	s_mov_b32 m0, s31
	global_load_lds_dwordx4 v132, s[66:67]
	s_add_i32 m0, s31, 0x2000
	s_nop 0
	global_load_lds_dwordx4 v136, s[66:67]
	s_barrier
	s_waitcnt lgkmcnt(0)
	s_setprio 1
	s_waitcnt lgkmcnt(0)
	v_mfma_f32_16x16x32_bf16 v[110:113], v[214:217], v[168:171], v[110:113]
	v_mfma_f32_16x16x32_bf16 v[106:109], v[222:225], v[168:171], v[106:109]
	v_mfma_f32_16x16x32_bf16 v[94:97], v[214:217], v[176:179], v[94:97]
	v_mfma_f32_16x16x32_bf16 v[90:93], v[222:225], v[176:179], v[90:93]
	v_mfma_f32_16x16x32_bf16 v[78:81], v[214:217], v[184:187], v[78:81]
	v_mfma_f32_16x16x32_bf16 v[74:77], v[222:225], v[184:187], v[74:77]
	v_mfma_f32_16x16x32_bf16 v[70:73], v[214:217], v[194:197], v[70:73]
	v_mfma_f32_16x16x32_bf16 v[66:69], v[222:225], v[194:197], v[66:69]
	v_mfma_f32_16x16x32_bf16 v[110:113], v[218:221], v[172:175], v[110:113]
	v_mfma_f32_16x16x32_bf16 v[106:109], v[226:229], v[172:175], v[106:109]
	v_mfma_f32_16x16x32_bf16 v[94:97], v[218:221], v[180:183], v[94:97]
	v_mfma_f32_16x16x32_bf16 v[90:93], v[226:229], v[180:183], v[90:93]
	v_mfma_f32_16x16x32_bf16 v[78:81], v[218:221], v[190:193], v[78:81]
	v_mfma_f32_16x16x32_bf16 v[74:77], v[226:229], v[190:193], v[74:77]
	v_mfma_f32_16x16x32_bf16 v[70:73], v[218:221], v[198:201], v[70:73]
	v_mfma_f32_16x16x32_bf16 v[66:69], v[226:229], v[198:201], v[66:69]
	s_setprio 0
	s_mov_b32 m0, s40
	s_barrier
	ds_read_b128 v[168:171], v150 offset:49152
	ds_read_b128 v[172:175], v150 offset:50176
	ds_read_b128 v[176:179], v150 offset:51200
	ds_read_b128 v[180:183], v150 offset:52224
	ds_read_b128 v[184:187], v150 offset:53248
	ds_read_b128 v[190:193], v150 offset:54272
	ds_read_b128 v[194:197], v150 offset:55296
	ds_read_b128 v[198:201], v150 offset:56320
	global_load_lds_dwordx4 v130, s[68:69]
	s_mov_b32 m0, s41
	s_nop 0
	global_load_lds_dwordx4 v134, s[68:69]
	s_waitcnt vmcnt(8)
	s_barrier
	s_waitcnt lgkmcnt(0)
	s_setprio 1
	s_waitcnt lgkmcnt(0)
	v_mfma_f32_16x16x32_bf16 v[62:65], v[152:155], v[168:171], v[62:65]
	v_mfma_f32_16x16x32_bf16 v[58:61], v[160:163], v[168:171], v[58:61]
	v_mfma_f32_16x16x32_bf16 v[54:57], v[152:155], v[176:179], v[54:57]
	v_mfma_f32_16x16x32_bf16 v[50:53], v[160:163], v[176:179], v[50:53]
	v_mfma_f32_16x16x32_bf16 v[38:41], v[152:155], v[184:187], v[38:41]
	v_mfma_f32_16x16x32_bf16 v[34:37], v[160:163], v[184:187], v[34:37]
	v_mfma_f32_16x16x32_bf16 v[22:25], v[152:155], v[194:197], v[22:25]
	v_mfma_f32_16x16x32_bf16 v[18:21], v[160:163], v[194:197], v[18:21]
	v_mfma_f32_16x16x32_bf16 v[62:65], v[156:159], v[172:175], v[62:65]
	v_mfma_f32_16x16x32_bf16 v[58:61], v[164:167], v[172:175], v[58:61]
	v_mfma_f32_16x16x32_bf16 v[54:57], v[156:159], v[180:183], v[54:57]
	v_mfma_f32_16x16x32_bf16 v[50:53], v[164:167], v[180:183], v[50:53]
	v_mfma_f32_16x16x32_bf16 v[38:41], v[156:159], v[190:193], v[38:41]
	v_mfma_f32_16x16x32_bf16 v[34:37], v[164:167], v[190:193], v[34:37]
	v_mfma_f32_16x16x32_bf16 v[22:25], v[156:159], v[198:201], v[22:25]
	v_mfma_f32_16x16x32_bf16 v[18:21], v[164:167], v[198:201], v[18:21]
	s_setprio 0
	s_barrier
	s_add_u32 s28, s28, 0x80080
	s_addc_u32 s29, s29, 0
	s_add_i32 s30, s30, s35
	s_mov_b32 m0, s30
	s_nop 0
	global_load_lds_dwordx4 v132, s[28:29]
	s_add_i32 m0, s30, 0x2000
	s_nop 0
	global_load_lds_dwordx4 v136, s[28:29]
	s_waitcnt vmcnt(6)
	s_barrier
	s_setprio 1
	v_mfma_f32_16x16x32_bf16 v[46:49], v[214:217], v[168:171], v[46:49]
	v_mfma_f32_16x16x32_bf16 v[42:45], v[222:225], v[168:171], v[42:45]
	ds_read_b128 v[152:155], v149
	v_mfma_f32_16x16x32_bf16 v[30:33], v[214:217], v[176:179], v[30:33]
	v_mfma_f32_16x16x32_bf16 v[26:29], v[222:225], v[176:179], v[26:29]
	ds_read_b128 v[156:159], v149 offset:1024
	v_mfma_f32_16x16x32_bf16 v[14:17], v[214:217], v[184:187], v[14:17]
	v_mfma_f32_16x16x32_bf16 v[10:13], v[222:225], v[184:187], v[10:13]
	ds_read_b128 v[160:163], v149 offset:2048
	v_mfma_f32_16x16x32_bf16 v[6:9], v[214:217], v[194:197], v[6:9]
	v_mfma_f32_16x16x32_bf16 v[2:5], v[222:225], v[194:197], v[2:5]
	ds_read_b128 v[164:167], v149 offset:3072
	v_mfma_f32_16x16x32_bf16 v[46:49], v[218:221], v[172:175], v[46:49]
	v_mfma_f32_16x16x32_bf16 v[42:45], v[226:229], v[172:175], v[42:45]
	v_mfma_f32_16x16x32_bf16 v[30:33], v[218:221], v[180:183], v[30:33]
	v_mfma_f32_16x16x32_bf16 v[26:29], v[226:229], v[180:183], v[26:29]
	v_mfma_f32_16x16x32_bf16 v[14:17], v[218:221], v[190:193], v[14:17]
	v_mfma_f32_16x16x32_bf16 v[10:13], v[226:229], v[190:193], v[10:13]
	v_mfma_f32_16x16x32_bf16 v[6:9], v[218:221], v[198:201], v[6:9]
	v_mfma_f32_16x16x32_bf16 v[2:5], v[226:229], v[198:201], v[2:5]
	s_setprio 0
	s_add_i32 s54, s54, 2
	s_add_u32 s26, s26, 0x100
	s_addc_u32 s27, s27, 0
	s_add_u32 s52, s52, 0x100
	s_addc_u32 s53, s53, 0
	s_cmp_gt_u32 s54, 29
	s_barrier
	s_cbranch_scc0 .LBB0_1369
	s_waitcnt lgkmcnt(0)
	v_lshl_add_u32 v152, s16, 8, v146
	v_lshl_or_b32 v154, s49, 8, v148
	v_ashrrev_i32_e32 v153, 31, v152
	v_ashrrev_i32_e32 v155, 31, v154
	v_lshlrev_b64 v[156:157], 12, v[152:153]
	v_lshl_add_u64 v[156:157], s[96:97], 0, v[156:157]
	v_lshlrev_b64 v[154:155], 1, v[154:155]
	v_lshl_add_u64 v[156:157], v[156:157], 0, v[154:155]
	v_cvt_pk_bf16_f32 v62, v62, v63
	v_cvt_pk_bf16_f32 v63, v64, v65
	v_cvt_pk_bf16_f32 v64, v58, v59
	v_add_co_u32_e32 v58, vcc, s45, v156
	v_cvt_pk_bf16_f32 v70, v70, v71
	v_cvt_pk_bf16_f32 v71, v72, v73
	v_cvt_pk_bf16_f32 v72, v66, v67
	v_lshl_add_u64 v[66:67], v[156:157], 0, s[6:7]
	v_addc_co_u32_e32 v59, vcc, 0, v157, vcc
	v_cvt_pk_bf16_f32 v46, v46, v47
	v_cvt_pk_bf16_f32 v47, v48, v49
	v_cvt_pk_bf16_f32 v48, v42, v43
	v_cvt_pk_bf16_f32 v49, v44, v45
	v_cvt_pk_bf16_f32 v110, v110, v111
	v_cvt_pk_bf16_f32 v111, v112, v113
	v_cvt_pk_bf16_f32 v112, v106, v107
	v_or_b32_e32 v106, 16, v152
	global_store_dwordx4 v[66:67], v[46:49], off offset:256
	v_ashrrev_i32_e32 v107, 31, v106
	v_cvt_pk_bf16_f32 v94, v94, v95
	v_add_co_u32_e32 v48, vcc, s46, v156
	v_cvt_pk_bf16_f32 v95, v96, v97
	v_cvt_pk_bf16_f32 v96, v90, v91
	v_or_b32_e32 v90, 32, v152
	v_lshl_add_u64 v[46:47], v[156:157], 0, s[10:11]
	v_addc_co_u32_e32 v49, vcc, 0, v157, vcc
	v_cvt_pk_bf16_f32 v30, v30, v31
	v_cvt_pk_bf16_f32 v31, v32, v33
	v_cvt_pk_bf16_f32 v32, v26, v27
	v_cvt_pk_bf16_f32 v33, v28, v29
	v_lshlrev_b64 v[106:107], 12, v[106:107]
	v_ashrrev_i32_e32 v91, 31, v90
	v_cvt_pk_bf16_f32 v78, v78, v79
	v_cvt_pk_bf16_f32 v79, v80, v81
	v_cvt_pk_bf16_f32 v80, v74, v75
	v_or_b32_e32 v74, 48, v152
	global_store_dwordx4 v[46:47], v[30:33], off offset:256
	v_cvt_pk_bf16_f32 v113, v108, v109
	v_lshl_add_u64 v[106:107], s[96:97], 0, v[106:107]
	v_add_co_u32_e32 v32, vcc, s47, v156
	v_lshlrev_b64 v[90:91], 12, v[90:91]
	v_ashrrev_i32_e32 v75, 31, v74
	v_lshl_add_u64 v[30:31], v[156:157], 0, s[12:13]
	v_addc_co_u32_e32 v33, vcc, 0, v157, vcc
	v_cvt_pk_bf16_f32 v14, v14, v15
	v_cvt_pk_bf16_f32 v15, v16, v17
	v_cvt_pk_bf16_f32 v16, v10, v11
	v_cvt_pk_bf16_f32 v17, v12, v13
	global_store_dwordx4 v[156:157], v[110:113], off offset:256
	v_cvt_pk_bf16_f32 v97, v92, v93
	v_lshl_add_u64 v[90:91], s[96:97], 0, v[90:91]
	v_lshl_add_u64 v[110:111], v[106:107], 0, v[154:155]
	v_lshlrev_b64 v[74:75], 12, v[74:75]
	global_store_dwordx4 v[30:31], v[14:17], off offset:256
	global_store_dwordx4 v[110:111], v[94:97], off offset:256
	v_cvt_pk_bf16_f32 v81, v76, v77
	v_add_co_u32_e32 v16, vcc, s48, v156
	v_lshl_add_u64 v[94:95], v[90:91], 0, v[154:155]
	v_lshl_add_u64 v[74:75], s[96:97], 0, v[74:75]
	v_addc_co_u32_e32 v17, vcc, 0, v157, vcc
	v_cvt_pk_bf16_f32 v126, v126, v127
	v_cvt_pk_bf16_f32 v127, v128, v129
	v_cvt_pk_bf16_f32 v128, v122, v123
	v_cvt_pk_bf16_f32 v129, v124, v125
	v_cvt_pk_bf16_f32 v106, v118, v119
	v_cvt_pk_bf16_f32 v107, v120, v121
	v_cvt_pk_bf16_f32 v108, v114, v115
	v_cvt_pk_bf16_f32 v109, v116, v117
	v_cvt_pk_bf16_f32 v90, v102, v103
	v_cvt_pk_bf16_f32 v91, v104, v105
	v_cvt_pk_bf16_f32 v92, v98, v99
	v_cvt_pk_bf16_f32 v93, v100, v101
	global_store_dwordx4 v[94:95], v[78:81], off offset:256
	v_cvt_pk_bf16_f32 v76, v82, v83
	v_cvt_pk_bf16_f32 v77, v84, v85
	v_lshl_add_u64 v[78:79], v[74:75], 0, v[154:155]
	v_cvt_pk_bf16_f32 v74, v86, v87
	v_cvt_pk_bf16_f32 v75, v88, v89
	v_cvt_pk_bf16_f32 v73, v68, v69
	v_cvt_pk_bf16_f32 v65, v60, v61
	v_cvt_pk_bf16_f32 v42, v54, v55
	v_cvt_pk_bf16_f32 v43, v56, v57
	v_cvt_pk_bf16_f32 v44, v50, v51
	v_cvt_pk_bf16_f32 v45, v52, v53
	v_cvt_pk_bf16_f32 v26, v38, v39
	v_cvt_pk_bf16_f32 v27, v40, v41
	v_cvt_pk_bf16_f32 v28, v34, v35
	v_cvt_pk_bf16_f32 v29, v36, v37
	v_lshl_add_u64 v[14:15], v[156:157], 0, s[14:15]
	v_cvt_pk_bf16_f32 v10, v22, v23
	v_cvt_pk_bf16_f32 v11, v24, v25
	v_cvt_pk_bf16_f32 v12, v18, v19
	v_cvt_pk_bf16_f32 v13, v20, v21
	v_cvt_pk_bf16_f32 v6, v6, v7
	v_cvt_pk_bf16_f32 v7, v8, v9
	v_cvt_pk_bf16_f32 v8, v2, v3
	v_cvt_pk_bf16_f32 v9, v4, v5
	s_and_b64 vcc, exec, s[0:1]
	s_mov_b32 s49, s18
	s_mov_b32 s16, s20
	s_mov_b64 s[28:29], s[24:25]
	s_mov_b64 s[26:27], s[22:23]
	global_store_dwordx4 v[156:157], v[126:129], off
	global_store_dwordx4 v[110:111], v[106:109], off
	global_store_dwordx4 v[94:95], v[90:93], off
	global_store_dwordx4 v[78:79], v[74:77], off
	global_store_dwordx4 v[78:79], v[70:73], off offset:256
	global_store_dwordx4 v[58:59], v[62:65], off
	global_store_dwordx4 v[48:49], v[42:45], off
	global_store_dwordx4 v[32:33], v[26:29], off
	global_store_dwordx4 v[16:17], v[10:13], off
	global_store_dwordx4 v[14:15], v[6:9], off offset:256
	s_cbranch_vccz .LBB0_1362
	s_waitcnt vmcnt(0)
	s_cmpk_gt_u32 s2, 0xff
	s_cbranch_scc1 .LBB0_1373
	s_barrier
